# static s_setprio 1 for waves 4-7 in the dilated-attention and MoBA item loops (reset at phase exit)
# speedup vs baseline: 1.0063x; 1.0063x over previous
.LBB0_232:
	v_readlane_b32 s0, v253, 56
	v_readlane_b32 s1, v253, 57
	s_andn2_b64 vcc, exec, s[0:1]
	s_cbranch_vccnz .LBB0_273
	s_ashr_i32 s0, s3, 1
	s_and_b32 s3, s0, 0xffffffe0
	s_add_u32 s12, s14, 0xe020000
	s_addc_u32 s13, s15, 0
	s_add_i32 s1, s3, 0x80
	v_and_b32_e32 v2, 63, v155
	v_and_b32_e32 v160, 31, v155
	s_add_u32 s11, s14, 0x28060000
	v_bfe_u32 v3, v155, 5, 1
	v_or_b32_e32 v4, s1, v160
	s_movk_i32 s16, 0x48
	v_lshlrev_b32_e32 v6, 2, v2
	s_addc_u32 s26, s15, 0
	v_lshlrev_b32_e32 v0, 3, v3
	v_mul_lo_u32 v4, v4, s16
	v_xor_b32_e32 v161, 0x80, v6
	s_add_u32 s27, s14, 0x2e060000
	v_mov_b32_e32 v6, 0x3080
	s_movk_i32 s17, 0x184
	v_cmp_gt_u32_e64 s[40:41], 32, v2
	s_addc_u32 s28, s15, 0
	v_add_lshl_u32 v2, v4, v0, 1
	s_add_i32 s14, s3, 0x60
	v_mul_u32_u24_e32 v4, 0x184, v160
	v_mad_u32_u24 v6, v160, s17, v6
	v_mov_b32_e32 v21, s0
	s_movk_i32 s0, 0xffe0
	v_lshlrev_b32_e32 v154, 2, v3
	v_or_b32_e32 v3, s14, v160
	s_add_i32 s15, s3, 0x90
	v_add_lshl_u32 v8, s1, v6, 1
	v_add_lshl_u32 v10, s1, v4, 1
	s_add_i32 s1, s3, 64
	v_add_lshl_u32 v12, s14, v4, 1
	v_add_lshl_u32 v14, s14, v6, 1
	s_add_i32 s14, s3, 32
	v_bfi_b32 v21, s0, v21, v155
	s_add_i32 s0, s3, 48
	v_add_lshl_u32 v7, s15, v6, 1
	v_add_lshl_u32 v9, s15, v4, 1
	v_or_b32_e32 v11, s1, v160
	s_add_i32 s15, s3, 0x70
	v_or_b32_e32 v16, s14, v160
	v_add_lshl_u32 v23, s0, v4, 1
	v_add_lshl_u32 v25, s0, v6, 1
	s_add_i32 s0, s3, 0x7fffffe0
	v_mul_lo_u32 v3, v3, s16
	v_mul_lo_u32 v11, v11, s16
	v_add_lshl_u32 v13, s15, v4, 1
	v_add_lshl_u32 v15, s15, v6, 1
	v_mul_lo_u32 v16, v16, s16
	s_add_i32 s15, s3, 0x50
	v_mul_lo_u32 v21, v21, s16
	v_or_b32_e32 v26, s0, v160
	s_or_b32 s0, s3, 16
	v_add_u32_e32 v5, 0, v0
	v_add_lshl_u32 v3, v3, v0, 1
	v_add_lshl_u32 v11, v11, v0, 1
	v_add_lshl_u32 v16, v16, v0, 1
	v_add_lshl_u32 v17, s1, v4, 1
	v_add_lshl_u32 v18, s15, v4, 1
	v_add_lshl_u32 v19, s1, v6, 1
	v_add_lshl_u32 v20, s15, v6, 1
	v_add_lshl_u32 v21, v21, v0, 1
	v_add_lshl_u32 v22, s14, v4, 1
	v_add_lshl_u32 v24, s14, v6, 1
	v_mul_lo_u32 v26, v26, s16
	v_add_lshl_u32 v27, s0, v6, 1
	v_add_lshl_u32 v6, s3, v6, 1
	v_add_lshl_u32 v28, s0, v4, 1
	v_add_lshl_u32 v4, s3, v4, 1
	v_add_lshl_u32 v26, v26, v0, 1
	v_add_u32_e32 v162, 0, v2
	v_add_u32_e32 v163, 0, v3
	v_add_u32_e32 v2, v5, v7
	v_add_u32_e32 v3, v5, v8
	v_add_u32_e32 v7, v5, v9
	v_add_u32_e32 v8, v5, v10
	v_add_u32_e32 v164, 0, v11
	v_add_u32_e32 v9, v5, v12
	v_add_u32_e32 v10, v5, v13
	v_add_u32_e32 v11, v5, v14
	v_add_u32_e32 v12, v5, v15
	v_add_u32_e32 v165, 0, v16
	v_add_u32_e32 v13, v5, v17
	v_add_u32_e32 v14, v5, v18
	v_add_u32_e32 v15, v5, v19
	v_add_u32_e32 v16, v5, v20
	v_add_u32_e32 v166, 0, v21
	v_add_u32_e32 v17, v5, v22
	v_add_u32_e32 v18, v5, v23
	v_add_u32_e32 v19, v5, v24
	v_add_u32_e32 v20, v5, v25
	v_add_u32_e32 v21, v5, v27
	v_add_u32_e32 v6, v5, v6
	v_add_u32_e32 v22, v5, v28
	v_add_u32_e32 v4, v5, v4
	v_readlane_b32 s0, v254, 32
	s_lshl_b32 s29, s2, 8
	v_lshlrev_b32_e32 v0, 1, v0
	v_add_u32_e32 v167, 0, v26
	v_lshlrev_b32_e32 v156, 1, v154
	v_add_u32_e32 v168, 0xd800, v2
	v_add_u32_e32 v169, 0xd800, v3
	v_add_u32_e32 v170, 0xd800, v7
	v_add_u32_e32 v171, 0xd800, v8
	v_add_u32_e32 v172, 0xd800, v9
	v_add_u32_e32 v173, 0xd800, v10
	v_add_u32_e32 v174, 0xd800, v11
	v_add_u32_e32 v175, 0xd800, v12
	v_add_u32_e32 v176, 0xd800, v13
	v_add_u32_e32 v177, 0xd800, v14
	v_add_u32_e32 v178, 0xd800, v15
	v_add_u32_e32 v179, 0xd800, v16
	v_add_u32_e32 v180, 0xd800, v17
	v_add_u32_e32 v181, 0xd800, v18
	v_add_u32_e32 v182, 0xd800, v19
	v_add_u32_e32 v183, 0xd800, v20
	v_add_u32_e32 v184, 0xd800, v21
	v_add_u32_e32 v185, 0xd800, v6
	v_add_u32_e32 v186, 0xd800, v22
	v_add_u32_e32 v187, 0xd800, v4
	v_readlane_b32 s30, v253, 58
	s_mov_b32 s33, s0
	v_readlane_b32 s1, v254, 33
	v_readlane_b32 s36, v253, 0
	s_cmp_ge_u32 s36, 0x100
	s_cbranch_scc0 .Lprio_0
	s_setprio 1
.Lprio_0:
	s_branch .LBB0_235
.LBB0_234:
	s_or_b64 exec, exec, s[16:17]
	s_add_i32 s30, s30, s29
	s_and_b64 vcc, exec, s[0:1]
	s_mov_b32 s33, s18
	s_barrier
	s_cbranch_vccnz .LBB0_273

.LBB0_273:
	s_setprio 0
	v_readlane_b32 s0, v254, 62
	s_add_i32 s2, s0, 5
	s_cmp_lt_i32 s2, s75
	s_cselect_b64 s[0:1], -1, 0
	s_and_b64 s[8:9], s[8:9], s[0:1]
	s_and_b64 vcc, exec, s[8:9]
	s_cbranch_vccz .LBB0_329
	v_readlane_b32 s8, v253, 1
	v_readlane_b32 s9, v253, 2
	s_and_b64 vcc, exec, s[8:9]
	s_mov_b64 s[12:13], 0
	s_cbranch_vccnz .LBB0_276
	v_mbcnt_lo_u32_b32 v0, -1, 0
	v_mbcnt_hi_u32_b32 v0, -1, v0
	s_nop 0
	v_cmp_eq_u32_e32 vcc, 0, v0
	s_and_b64 s[12:13], vcc, exec

.LBB0_628:
	v_readlane_b32 s0, v254, 6
	v_readlane_b32 s1, v254, 7
	s_andn2_b64 vcc, exec, s[0:1]
	s_cbranch_vccnz .LBB0_819
	v_readlane_b32 s0, v254, 41
	v_readlane_b32 s2, v253, 0
	s_nop 0
	v_mov_b32_e32 v0, s0
	s_waitcnt vmcnt(0)
	ds_read_b64 v[2:3], v0
	v_mbcnt_lo_u32_b32 v0, -1, 0
	v_mbcnt_hi_u32_b32 v0, -1, v0
	s_waitcnt lgkmcnt(0)
	v_readfirstlane_b32 s0, v2
	v_add_u32_e32 v2, s2, v0
	v_readlane_b32 s2, v254, 2
	v_readlane_b32 s3, v254, 3
	v_readfirstlane_b32 s1, v3
	s_and_b64 vcc, exec, s[2:3]
	s_cbranch_vccz .LBB0_819
	v_and_b32_e32 v3, 63, v2
	v_lshlrev_b32_e32 v0, 3, v2
	v_ashrrev_i32_e32 v9, 3, v2
	s_movk_i32 s11, 0x48
	v_and_b32_e32 v4, 56, v0
	v_cmp_eq_u32_e64 s[42:43], 0, v3
	v_lshlrev_b32_e32 v12, 2, v3
	v_cmp_gt_u32_e64 s[44:45], 32, v3
	s_movk_i32 s16, 0x1800
	v_mul_lo_u32 v3, v9, s11
	v_lshlrev_b32_e32 v10, 2, v9
	v_mad_i64_i32 v[136:137], s[14:15], v9, s16, 0
	v_add_lshl_u32 v9, v3, v4, 1
	v_add_u32_e32 v3, 0x200, v2
	v_ashrrev_i32_e32 v3, 3, v3
	v_mad_i64_i32 v[138:139], s[14:15], v3, s16, 0
	v_mul_lo_u32 v3, v3, s11
	v_xor_b32_e32 v164, 0x80, v12
	v_add_lshl_u32 v12, v3, v4, 1
	v_add_u32_e32 v3, 0x400, v2
	v_ashrrev_i32_e32 v3, 3, v3
	v_mad_i64_i32 v[140:141], s[14:15], v3, s16, 0
	v_mul_lo_u32 v3, v3, s11
	v_add_lshl_u32 v13, v3, v4, 1
	v_add_u32_e32 v3, 0x600, v2
	v_ashrrev_i32_e32 v3, 3, v3
	v_mad_i64_i32 v[142:143], s[14:15], v3, s16, 0
	v_mul_lo_u32 v3, v3, s11
	v_add_lshl_u32 v14, v3, v4, 1
	v_or_b32_e32 v3, 1, v10
	v_mad_i64_i32 v[146:147], s[14:15], v3, s16, 0
	v_or_b32_e32 v3, 2, v10
	v_mad_i64_i32 v[148:149], s[14:15], v3, s16, 0
	v_or_b32_e32 v3, 3, v10
	v_add_u32_e32 v11, 0x104, v10
	v_mad_i64_i32 v[150:151], s[14:15], v3, s16, 0
	v_mul_u32_u24_e32 v3, 0x104, v4
	v_add_lshl_u32 v15, v3, v10, 1
	v_add_lshl_u32 v16, v3, v11, 1
	v_mov_b32_e32 v3, 0x208
	s_movk_i32 s11, 0x104
	s_add_u32 s2, s0, 0x45be0a00
	v_mad_u32_u24 v3, v4, s11, v3
	s_addc_u32 s3, s1, 0
	v_add_lshl_u32 v17, v3, v10, 1
	v_add_lshl_u32 v18, v3, v11, 1
	v_mov_b32_e32 v3, 0x410
	s_add_u32 s8, s0, 0xe020000
	v_mad_u32_u24 v3, v4, s11, v3
	v_bfe_u32 v8, v2, 5, 1
	s_addc_u32 s9, s1, 0
	v_add_lshl_u32 v19, v3, v10, 1
	v_add_lshl_u32 v20, v3, v11, 1
	v_mov_b32_e32 v3, 0x618
	v_lshlrev_b32_e32 v0, 3, v8
	s_add_u32 s12, s0, 0x4dce0a00
	v_mad_u32_u24 v3, v4, s11, v3
	v_and_b32_e32 v5, 31, v2
	v_cmp_eq_u32_e64 s[40:41], 0, v2
	v_add_u32_e32 v162, 0x100, v2
	v_lshlrev_b64 v[6:7], v2, -1
	s_addc_u32 s13, s1, 0
	v_mad_i64_i32 v[144:145], s[14:15], v10, s16, 0
	v_add_lshl_u32 v10, v3, v10, 1
	v_add_lshl_u32 v11, v3, v11, 1
	v_add_u32_e32 v165, 0x300, v2
	v_add_u32_e32 v166, 0x500, v2
	v_add_u32_e32 v167, 0x700, v2
	v_add_u32_e32 v168, 0x900, v2
	v_add_u32_e32 v169, 0xb00, v2
	v_add_u32_e32 v170, 0xd00, v2
	v_add_u32_e32 v171, 0xf00, v2
	v_add_u32_e32 v172, 0x1100, v2
	v_add_u32_e32 v173, 0x1300, v2
	v_add_u32_e32 v174, 0x1500, v2
	v_add_u32_e32 v175, 0x1700, v2
	v_add_u32_e32 v176, 0x1900, v2
	v_add_u32_e32 v177, 0x1b00, v2
	v_add_u32_e32 v178, 0x1d00, v2
	v_add_u32_e32 v179, 0x1f00, v2
	v_lshl_add_u64 v[2:3], s[0:1], 0, v[0:1]
	s_mov_b64 s[0:1], 0x45ce0a00
	v_not_b32_e32 v133, v7
	v_not_b32_e32 v132, v6
	v_lshlrev_b32_e32 v6, 4, v8
	v_mov_b32_e32 v7, v1
	v_mul_u32_u24_e32 v21, 0x104, v5
	v_lshl_add_u64 v[152:153], v[2:3], 0, s[0:1]
	v_mul_u32_u24_e32 v2, 0x90, v5
	v_readlane_b32 s0, v254, 46
	v_lshl_add_u64 v[134:135], s[8:9], 0, v[6:7]
	v_mul_u32_u24_e32 v7, 0x48, v5
	v_add3_u32 v181, v2, v6, s0
	v_lshlrev_b32_e32 v2, 1, v21
	v_readlane_b32 s0, v254, 47
	v_lshlrev_b32_e32 v8, 2, v8
	v_add_lshl_u32 v7, v0, v7, 1
	s_movk_i32 s11, 0x2000
	v_add3_u32 v183, v0, v2, s0
	v_readlane_b32 s0, v254, 32
	v_or_b32_e32 v163, 0xffffff00, v5
	v_or_b32_e32 v180, 0xe0, v5
	v_cmp_gt_i32_e64 s[46:47], s11, v179
	v_sub_u32_e32 v182, 0, v8
	v_lshlrev_b32_e32 v154, 1, v4
	v_add_u32_e32 v184, 0, v9
	v_add_u32_e32 v185, 0, v12
	v_add_u32_e32 v186, 0, v13
	v_add_u32_e32 v187, 0, v14
	v_add_u32_e32 v188, 0, v15
	v_add_u32_e32 v189, 0, v16
	v_add_u32_e32 v190, 0, v17
	v_add_u32_e32 v191, 0, v18
	v_add_u32_e32 v192, 0, v19
	v_add_u32_e32 v193, 0, v20
	v_add_u32_e32 v194, 0, v10
	v_add_u32_e32 v195, 0, v11
	v_add_u32_e32 v196, 0, v7
	s_mov_b32 s11, s0
	v_readlane_b32 s1, v254, 33
	v_readlane_b32 s36, v253, 0
	s_cmp_ge_u32 s36, 0x100
	s_cbranch_scc0 .Lprio_1
	s_setprio 1
.Lprio_1:
	s_branch .LBB0_632
.LBB0_631:
	v_readlane_b32 s0, v253, 3
	v_readlane_b32 s1, v253, 4
	s_waitcnt lgkmcnt(0)
	s_barrier
	s_load_dword s0, s[0:1], 0x0
	s_waitcnt lgkmcnt(0)
	s_add_i32 s11, s11, s0
	s_cmpk_gt_i32 s11, 0x3ff
	s_cbranch_scc1 .LBB0_819

.LBB0_819:
	s_setprio 0
	v_readlane_b32 s0, v254, 8
	v_readlane_b32 s1, v254, 9
	s_and_b64 vcc, exec, s[0:1]
	s_cbranch_vccz .LBB0_875
	v_readlane_b32 s0, v253, 1
	v_readlane_b32 s1, v253, 2
	s_and_b64 vcc, exec, s[0:1]
	s_mov_b64 s[8:9], 0
	s_cbranch_vccnz .LBB0_822
	v_mbcnt_lo_u32_b32 v0, -1, 0
	v_mbcnt_hi_u32_b32 v0, -1, v0
	s_nop 0
	v_cmp_eq_u32_e32 vcc, 0, v0
	s_and_b64 s[8:9], vcc, exec
